# speedup vs baseline: 1.0141x; 1.0021x over previous
_Z7kfinal3PKDF16_PKfS2_S2_PK15HIP_vector_typeIjLj4EES2_Pf:
	s_load_dwordx2 s[20:21], s[0:1], 0x20
	v_lshrrev_b32_e32 v48, 6, v0
	s_bfe_u32 s24, s2, 0x20003
	s_mul_i32 s3, s24, 0x28800
	v_lshlrev_b32_e32 v118, 10, v48
	v_and_b32_e32 v1, 63, v0
	s_waitcnt lgkmcnt(0)
	s_add_u32 s6, s20, s3
	v_add_u32_e32 v2, 0, v118
	s_addc_u32 s7, s21, 0
	s_mov_b32 s50, s6
	s_mov_b32 s51, s7
	s_mov_b32 s45, s2
	v_mov_b32_e32 v47, 0
	v_lshlrev_b32_e32 v46, 4, v1
	v_accvgpr_write_b32 a72, v2
	v_add_u32_e32 v8, 0xc600, v2
	v_and_b32_e32 v2, 0x1c0, v0
	v_lshl_add_u64 v[4:5], s[6:7], 0, v[46:47]
	v_lshlrev_b32_e32 v2, 4, v2
	v_mov_b32_e32 v3, v47
	v_readfirstlane_b32 s3, v8
	v_lshl_add_u64 v[6:7], v[4:5], 0, v[2:3]
	s_mov_b32 m0, s3
	v_or_b32_e32 v49, 8, v48
	global_load_lds_dwordx4 v[6:7], off
	s_movk_i32 s3, 0x280
	v_cmp_gt_u32_e64 s[4:5], s3, v0
	v_lshlrev_b32_e32 v90, 10, v49
	s_and_saveexec_b64 s[8:9], s[4:5]
	s_cbranch_execz .LBB3_2
	v_add_u32_e32 v3, 0, v90
	v_add_u32_e32 v3, 0xc600, v3
	v_mov_b32_e32 v91, v47
	v_readfirstlane_b32 s3, v3
	v_lshl_add_u64 v[6:7], v[4:5], 0, v[90:91]
	s_mov_b32 m0, s3
	s_nop 0
	global_load_lds_dwordx4 v[6:7], off

.LBB3_20:
	s_or_b64 exec, exec, s[6:7]
	s_load_dwordx2 s[12:13], s[0:1], 0x30
	v_min_u32_e32 v47, 27, v50
	v_min_u32_e32 v2, 3, v48
	v_or_b32_e32 v56, 24, v2
	v_lshrrev_b32_e32 v122, 4, v1
	v_and_b32_e32 v93, 15, v0
	v_lshrrev_b32_e32 v120, 8, v0
	s_lshl_b32 s18, s24, 18
	v_and_b32_e32 v121, 3, v48
	v_lshl_or_b32 v123, v120, 4, v93
	s_movk_i32 s0, 0x42
	s_cmp_lg_u32 0, -1
	v_mad_u32_u24 v1, v121, s0, v123
	s_cselect_b32 s0, 0, 0
	v_lshlrev_b32_e32 v2, 7, v1
	v_bitop3_b32 v3, v1, v122, 7 bitop3:0x6c
	v_add_u32_e32 v1, 33, v1
	s_add_i32 s1, s0, 0xc600
	v_lshl_or_b32 v126, v3, 4, v2
	v_lshlrev_b32_e32 v2, 7, v1
	v_bitop3_b32 v1, v1, v122, 7 bitop3:0x6c
	v_add_u32_e32 v124, s1, v46
	s_add_i32 s1, s0, 0xca00
	v_lshl_or_b32 v127, v1, 4, v2
	v_add_u32_e32 v1, s1, v46
	s_add_i32 s1, s0, 0xce00
	s_waitcnt vmcnt(6)
	s_waitcnt lgkmcnt(0)
	s_barrier
	ds_read_b128 v[42:45], v124
	ds_read_b128 v[38:41], v1
	v_add_u32_e32 v1, s1, v46
	s_add_i32 s1, s0, 0xd200
	ds_read_b128 v[34:37], v1
	v_add_u32_e32 v1, s1, v46
	s_add_i32 s1, s0, 0xd600
	ds_read_b128 v[30:33], v1
	v_add_u32_e32 v1, s1, v46
	s_add_i32 s1, s0, 0xda00
	ds_read_b128 v[26:29], v1
	v_add_u32_e32 v1, s1, v46
	s_add_i32 s1, s0, 0xde00
	ds_read_b128 v[22:25], v1
	v_add_u32_e32 v1, s1, v46
	s_add_i32 s1, s0, 0xe200
	ds_read_b128 v[10:13], v1
	v_add_u32_e32 v1, s1, v46
	s_add_i32 s1, s0, 0xe600
	ds_read_b128 v[6:9], v1
	v_add_u32_e32 v1, s1, v46
	ds_read_b128 v[2:5], v1
	v_add_u32_e32 v1, s0, v126
	ds_read_b128 v[14:17], v1
	v_add_u32_e32 v1, s0, v127
	s_add_i32 s0, s0, 0xea00
	v_add_u32_e32 v125, s0, v46
	s_lshl_b32 s0, s24, 20
	s_add_u32 s10, s2, s0
	v_mov_b32_e32 v95, 0
	v_lshlrev_b32_e32 v0, 4, v0
	ds_read_b128 v[18:21], v1
	s_addc_u32 s11, s3, 0
	v_lshlrev_b32_e32 v91, 10, v47
	v_and_b32_e32 v0, 0x1c00, v0
	v_mov_b32_e32 v1, v95
	v_mov_b32_e32 v47, 0x28800
	s_add_u32 s0, s10, 0x400000
	v_mad_u64_u32 v[54:55], s[2:3], s24, v47, v[0:1]
	s_addc_u32 s1, s11, 0
	v_lshlrev_b32_e32 v48, 2, v94
	v_mov_b32_e32 v49, v95
	v_lshlrev_b32_e32 v50, 2, v96
	v_mov_b32_e32 v51, v95
	v_lshlrev_b32_e32 v52, 2, v98
	v_mov_b32_e32 v53, v95
	v_or_b32_e32 v54, v54, v46
	v_lshlrev_b32_e32 v46, 2, v100
	v_mov_b32_e32 v47, v95
	s_waitcnt lgkmcnt(0)
	v_lshl_add_u64 v[0:1], s[0:1], 0, v[48:49]
	v_lshl_add_u64 v[106:107], s[0:1], 0, v[50:51]
	v_lshl_add_u64 v[110:111], s[0:1], 0, v[52:53]
	v_lshl_add_u64 v[112:113], s[10:11], 0, v[46:47]
	v_lshl_add_u64 v[114:115], s[0:1], 0, v[46:47]
	v_lshl_add_u64 v[46:47], s[20:21], 0, v[54:55]
	s_mov_b64 s[0:1], 0xd000
	v_lshl_add_u64 v[116:117], v[46:47], 0, s[0:1]
	s_movk_i32 s0, 0xc000
	s_movk_i32 s2, 0xe000
	s_mov_b32 s19, 0
	v_lshl_add_u64 v[102:103], s[10:11], 0, v[48:49]
	v_mov_b32_e32 v97, v95
	v_mov_b32_e32 v99, v95
	v_mov_b32_e32 v101, v95
	v_lshlrev_b32_e32 v119, 10, v56
	v_lshl_add_u64 v[104:105], s[10:11], 0, v[50:51]
	v_lshl_add_u64 v[108:109], s[10:11], 0, v[52:53]
	s_mov_b32 s20, 1
	s_mov_b32 s1, -1
	s_mov_b32 s3, -1
	s_add_i32 s17, 0, 0x16000
	s_add_i32 s16, 0, 0x1d000
	s_mov_b64 s[6:7], 0x4800
	s_cmp_ge_u32 s42, 0x1000
	s_cbranch_scc0 .Lk4_noprio
	s_setprio 1
